# same code as the coalesced-A version with the metadata sgpr_count made truthful
# speedup vs baseline: 1.0167x; 1.0097x over previous
amdhsa.kernels:
  - .agpr_count:     16
    .args:
      - .actual_access:  read_only
        .address_space:  global
        .offset:         0
        .size:           8
        .value_kind:     global_buffer
      - .actual_access:  read_only
        .address_space:  global
        .offset:         8
        .size:           8
        .value_kind:     global_buffer
      - .actual_access:  read_only
        .address_space:  global
        .offset:         16
        .size:           8
        .value_kind:     global_buffer
      - .actual_access:  read_only
        .address_space:  global
        .offset:         24
        .size:           8
        .value_kind:     global_buffer
      - .actual_access:  read_only
        .address_space:  global
        .offset:         32
        .size:           8
        .value_kind:     global_buffer
      - .actual_access:  read_only
        .address_space:  global
        .offset:         40
        .size:           8
        .value_kind:     global_buffer
      - .actual_access:  write_only
        .address_space:  global
        .offset:         48
        .size:           8
        .value_kind:     global_buffer
      - .actual_access:  write_only
        .address_space:  global
        .offset:         56
        .size:           8
        .value_kind:     global_buffer
      - .actual_access:  write_only
        .address_space:  global
        .offset:         64
        .size:           8
        .value_kind:     global_buffer
      - .actual_access:  write_only
        .address_space:  global
        .offset:         72
        .size:           8
        .value_kind:     global_buffer
      - .actual_access:  write_only
        .address_space:  global
        .offset:         80
        .size:           8
        .value_kind:     global_buffer
      - .actual_access:  write_only
        .address_space:  global
        .offset:         88
        .size:           8
        .value_kind:     global_buffer
    .group_segment_fixed_size: 50176
    .kernarg_segment_align: 8
    .kernarg_segment_size: 96
    .language:       OpenCL C
    .language_version:
      - 2
      - 0
    .max_flat_workgroup_size: 256
    .name:           _Z7na_prepPKfS0_S0_S0_S0_S0_PDF16_PhS1_PfS3_S3_
    .private_segment_fixed_size: 0
    .sgpr_count:     23
    .sgpr_spill_count: 0
    .symbol:         _Z7na_prepPKfS0_S0_S0_S0_S0_PDF16_PhS1_PfS3_S3_.kd
    .uniform_work_group_size: 1
    .uses_dynamic_stack: false
    .vgpr_count:     116
    .vgpr_spill_count: 0
    .wavefront_size: 64
  - .agpr_count:     0
    .args:
      - .address_space:  global
        .offset:         0
        .size:           8
        .value_kind:     global_buffer
      - .actual_access:  read_only
        .address_space:  global
        .offset:         8
        .size:           8
        .value_kind:     global_buffer
      - .actual_access:  read_only
        .address_space:  global
        .offset:         16
        .size:           8
        .value_kind:     global_buffer
      - .actual_access:  read_only
        .address_space:  global
        .offset:         24
        .size:           8
        .value_kind:     global_buffer
      - .actual_access:  read_only
        .address_space:  global
        .offset:         32
        .size:           8
        .value_kind:     global_buffer
      - .actual_access:  read_only
        .address_space:  global
        .offset:         40
        .size:           8
        .value_kind:     global_buffer
      - .actual_access:  read_only
        .address_space:  global
        .offset:         48
        .size:           8
        .value_kind:     global_buffer
      - .actual_access:  write_only
        .address_space:  global
        .offset:         56
        .size:           8
        .value_kind:     global_buffer
    .group_segment_fixed_size: 162048
    .kernarg_segment_align: 8
    .kernarg_segment_size: 64
    .language:       OpenCL C
    .language_version:
      - 2
      - 0
    .max_flat_workgroup_size: 512
    .name:           _Z7na_mainPKDF16_PKhS0_PKfS4_S4_S4_Pf
    .private_segment_fixed_size: 0
    .sgpr_count:     42
    .sgpr_spill_count: 0
    .symbol:         _Z7na_mainPKDF16_PKhS0_PKfS4_S4_S4_Pf.kd
    .uniform_work_group_size: 1
    .uses_dynamic_stack: false
    .vgpr_count:     252
    .vgpr_spill_count: 0
    .wavefront_size: 64
